# speedup vs baseline: 1.0036x; 1.0036x over previous
.Lat_u0:
	ds_read_b128 v[112:115], v164
	v_mfma_i32_32x32x32_i8 v[84:99], v[242:245], v[140:143], v[84:99]
	ds_read_b128 v[116:119], v195 offset:6144
	ds_read_b128 v[120:123], v196 offset:6144
	s_cmp_gt_u32 s43, 29
	s_cbranch_scc1 .Lat_nok0
	s_add_i32 m0, s31, 49152
	ds_read_b128 v[124:127], v195 offset:4096
	global_load_lds_dwordx4 v252, s[60:61] nt
	s_add_i32 m0, s31, 57344
	v_mfma_i32_32x32x32_i8 v[84:99], v[246:249], v[144:147], v[84:99]
	global_load_lds_dwordx4 v254, s[60:61] nt
.Lat_k0:
	ds_read_b128 v[128:131], v196 offset:4096
	v_mfma_i32_32x32x32_i8 v[84:99], v[202:205], v[148:151], v[84:99]
	ds_read_b128 v[202:205], v195
	v_mfma_i32_32x32x32_i8 v[84:99], v[206:209], v[152:155], v[84:99]
	ds_read_b128 v[206:209], v196
	v_mfma_i32_32x32x32_i8 v[84:99], v[210:213], v[156:159], v[84:99]
	ds_read_b128 v[210:213], v195 offset:2048
	v_mfma_i32_32x32x32_i8 v[84:99], v[214:217], v[160:163], v[84:99]
	ds_read_b128 v[214:217], v196 offset:2048
	v_readlane_b32 s50, v182, s43
	s_waitcnt lgkmcnt(6)
	v_mfma_f32_32x32x64_f8f6f4 v[2:17], v[108:115], v[116:123], v[2:17]
	ds_read_b128 v[218:221], v185 offset:32768
	ds_read_b128 v[222:225], v186 offset:32768
	ds_read_b128 v[242:245], v187 offset:32768
	ds_read_b128 v[246:249], v188 offset:32768
	v_mul_f32_e32 v250, s50, v71
	v_fmamk_f32 v251, v250, 0xcb400000, v200
	s_cmp_gt_u32 s43, 30
	s_cbranch_scc1 .Lat_nov0
	s_add_i32 m0, s31, 32768
	v_fma_f32 v84, v84, v250, v251
	global_load_lds_dwordx4 v255, s[60:61] nt
	s_add_i32 m0, s31, 40960
	v_fma_f32 v85, v85, v250, v251
	global_load_lds_dwordx4 v201, s[60:61] nt

.Lat_u1:
	ds_read_b128 v[104:107], v164 offset:8192
	v_mfma_i32_32x32x32_i8 v[84:99], v[242:245], v[140:143], v[84:99]
	ds_read_b128 v[116:119], v195 offset:22528
	ds_read_b128 v[120:123], v196 offset:22528
	s_add_i32 m0, s31, 65536
	ds_read_b128 v[124:127], v195 offset:20480
	global_load_lds_dwordx4 v252, s[60:61] nt
	s_add_i32 m0, s31, 73728
	v_mfma_i32_32x32x32_i8 v[84:99], v[246:249], v[144:147], v[84:99]
	global_load_lds_dwordx4 v254, s[60:61] nt
	ds_read_b128 v[128:131], v196 offset:20480
	v_mfma_i32_32x32x32_i8 v[84:99], v[202:205], v[148:151], v[84:99]
	ds_read_b128 v[202:205], v195 offset:16384
	v_mfma_i32_32x32x32_i8 v[84:99], v[206:209], v[152:155], v[84:99]
	ds_read_b128 v[206:209], v196 offset:16384
	v_mfma_i32_32x32x32_i8 v[84:99], v[210:213], v[156:159], v[84:99]
	ds_read_b128 v[210:213], v195 offset:18432
	v_mfma_i32_32x32x32_i8 v[84:99], v[214:217], v[160:163], v[84:99]
	ds_read_b128 v[214:217], v196 offset:18432
	v_readlane_b32 s50, v182, s43
	s_waitcnt lgkmcnt(6)
	v_mfma_f32_32x32x64_f8f6f4 v[2:17], v[100:107], v[116:123], v[2:17]
	ds_read_b128 v[218:221], v185
	ds_read_b128 v[222:225], v186
	ds_read_b128 v[242:245], v187
	ds_read_b128 v[246:249], v188
	v_mul_f32_e32 v250, s50, v71
	v_fmamk_f32 v251, v250, 0xcb400000, v200
	s_mov_b32 m0, s31
	v_fma_f32 v84, v84, v250, v251
	global_load_lds_dwordx4 v255, s[60:61] nt
	s_add_i32 m0, s31, 8192
	v_fma_f32 v85, v85, v250, v251
	global_load_lds_dwordx4 v201, s[60:61] nt
	v_fma_f32 v86, v86, v250, v251
	v_fma_f32 v87, v87, v250, v251
	v_exp_f32_e32 v84, v84
	v_exp_f32_e32 v85, v85
	v_exp_f32_e32 v86, v86
	v_exp_f32_e32 v87, v87
	v_fma_f32 v88, v88, v250, v251
	v_fma_f32 v89, v89, v250, v251
	v_fma_f32 v90, v90, v250, v251
	v_fma_f32 v91, v91, v250, v251
	s_waitcnt lgkmcnt(8)
	v_mfma_f32_32x32x64_f8f6f4 v[18:33], v[100:107], v[124:131], v[18:33]
	v_add_f32_e32 v67, v84, v85
	v_add_f32_e32 v68, v86, v87
	v_exp_f32_e32 v88, v88
	v_exp_f32_e32 v89, v89
	v_exp_f32_e32 v90, v90
	v_exp_f32_e32 v91, v91
	v_add_f32_e32 v67, v67, v68
	v_cvt_pk_fp8_f32 v108, v84, v85
	v_cvt_pk_fp8_f32 v108, v86, v87 op_sel:[0,0,1]
	v_fma_f32 v92, v92, v250, v251
	v_fma_f32 v93, v93, v250, v251
	v_fma_f32 v94, v94, v250, v251
	v_fma_f32 v95, v95, v250, v251
	v_add_f32_e32 v68, v88, v89
	v_add_f32_e32 v69, v90, v91
	s_waitcnt lgkmcnt(6)
	v_mfma_f32_32x32x64_f8f6f4 v[50:65], v[100:107], v[202:209], v[50:65]
	ds_read_b128 v[202:205], v189
	ds_read_b128 v[206:209], v190
	v_exp_f32_e32 v92, v92
	v_exp_f32_e32 v93, v93
	v_exp_f32_e32 v94, v94
	v_exp_f32_e32 v95, v95
	v_add_f32_e32 v68, v68, v69
	v_cvt_pk_fp8_f32 v109, v88, v89
	v_cvt_pk_fp8_f32 v109, v90, v91 op_sel:[0,0,1]
	v_fma_f32 v96, v96, v250, v251
	v_fma_f32 v97, v97, v250, v251
	v_fma_f32 v98, v98, v250, v251
	v_fma_f32 v99, v99, v250, v251
	v_add_f32_e32 v67, v67, v68
	v_add_f32_e32 v68, v92, v93
	v_add_f32_e32 v69, v94, v95
	s_waitcnt lgkmcnt(6)
	v_mfma_f32_32x32x64_f8f6f4 v[34:49], v[100:107], v[210:217], v[34:49]
	ds_read_b128 v[210:213], v191
	ds_read_b128 v[214:217], v192
	v_exp_f32_e32 v96, v96
	v_exp_f32_e32 v97, v97
	v_exp_f32_e32 v98, v98
	v_exp_f32_e32 v99, v99
	v_add_f32_e32 v68, v68, v69
	v_cvt_pk_fp8_f32 v110, v92, v93
	v_cvt_pk_fp8_f32 v110, v94, v95 op_sel:[0,0,1]
	v_add_f32_e32 v67, v67, v68
	v_add_f32_e32 v68, v96, v97
	v_add_f32_e32 v69, v98, v99
	s_add_u32 s60, s60, 0x4000
	s_addc_u32 s61, s61, 0
	v_add_f32_e32 v68, v68, v69
	v_cvt_pk_fp8_f32 v111, v96, v97
	v_cvt_pk_fp8_f32 v111, v98, v99 op_sel:[0,0,1]
	v_add_f32_e32 v67, v67, v68
	ds_write_b128 v194, v[108:111]
	v_max_f32_e32 v72, v72, v67
	v_add_f32_e32 v66, v66, v67
	s_add_i32 s43, s43, 1
	s_waitcnt lgkmcnt(7)
	v_mfma_i32_32x32x32_i8 v[84:99], v[218:221], v[132:135], v[226:241]
	v_mfma_i32_32x32x32_i8 v[84:99], v[222:225], v[136:139], v[84:99]
	s_waitcnt vmcnt(2) lgkmcnt(0)
	s_barrier
.Lat_u2:
	ds_read_b128 v[112:115], v164
	v_mfma_i32_32x32x32_i8 v[84:99], v[242:245], v[140:143], v[84:99]
	ds_read_b128 v[116:119], v195 offset:38912
	ds_read_b128 v[120:123], v196 offset:38912
	s_add_i32 m0, s31, 81920
	ds_read_b128 v[124:127], v195 offset:36864
	global_load_lds_dwordx4 v252, s[60:61] nt
	s_add_i32 m0, s31, 90112
	v_mfma_i32_32x32x32_i8 v[84:99], v[246:249], v[144:147], v[84:99]
	global_load_lds_dwordx4 v254, s[60:61] nt
	ds_read_b128 v[128:131], v196 offset:36864
	v_mfma_i32_32x32x32_i8 v[84:99], v[202:205], v[148:151], v[84:99]
	ds_read_b128 v[202:205], v195 offset:32768
	v_mfma_i32_32x32x32_i8 v[84:99], v[206:209], v[152:155], v[84:99]
	ds_read_b128 v[206:209], v196 offset:32768
	v_mfma_i32_32x32x32_i8 v[84:99], v[210:213], v[156:159], v[84:99]
	ds_read_b128 v[210:213], v195 offset:34816
	v_mfma_i32_32x32x32_i8 v[84:99], v[214:217], v[160:163], v[84:99]
	ds_read_b128 v[214:217], v196 offset:34816
	v_readlane_b32 s50, v182, s43
	s_waitcnt lgkmcnt(6)
	v_mfma_f32_32x32x64_f8f6f4 v[2:17], v[108:115], v[116:123], v[2:17]
	ds_read_b128 v[218:221], v185 offset:16384
	ds_read_b128 v[222:225], v186 offset:16384
	ds_read_b128 v[242:245], v187 offset:16384
	ds_read_b128 v[246:249], v188 offset:16384
	v_mul_f32_e32 v250, s50, v71
	v_fmamk_f32 v251, v250, 0xcb400000, v200
	s_add_i32 m0, s31, 16384
	v_fma_f32 v84, v84, v250, v251
	global_load_lds_dwordx4 v255, s[60:61] nt
	s_add_i32 m0, s31, 24576
	v_fma_f32 v85, v85, v250, v251
	global_load_lds_dwordx4 v201, s[60:61] nt
	v_fma_f32 v86, v86, v250, v251
	v_fma_f32 v87, v87, v250, v251
	v_exp_f32_e32 v84, v84
	v_exp_f32_e32 v85, v85
	v_exp_f32_e32 v86, v86
	v_exp_f32_e32 v87, v87
	v_fma_f32 v88, v88, v250, v251
	v_fma_f32 v89, v89, v250, v251
	v_fma_f32 v90, v90, v250, v251
	v_fma_f32 v91, v91, v250, v251
	s_waitcnt lgkmcnt(8)
	v_mfma_f32_32x32x64_f8f6f4 v[18:33], v[108:115], v[124:131], v[18:33]
	v_add_f32_e32 v67, v84, v85
	v_add_f32_e32 v68, v86, v87
	v_exp_f32_e32 v88, v88
	v_exp_f32_e32 v89, v89
	v_exp_f32_e32 v90, v90
	v_exp_f32_e32 v91, v91
	v_add_f32_e32 v67, v67, v68
	v_cvt_pk_fp8_f32 v100, v84, v85
	v_cvt_pk_fp8_f32 v100, v86, v87 op_sel:[0,0,1]
	v_fma_f32 v92, v92, v250, v251
	v_fma_f32 v93, v93, v250, v251
	v_fma_f32 v94, v94, v250, v251
	v_fma_f32 v95, v95, v250, v251
	v_add_f32_e32 v68, v88, v89
	v_add_f32_e32 v69, v90, v91
	s_waitcnt lgkmcnt(6)
	v_mfma_f32_32x32x64_f8f6f4 v[50:65], v[108:115], v[202:209], v[50:65]
	ds_read_b128 v[202:205], v189 offset:16384
	ds_read_b128 v[206:209], v190 offset:16384
	v_exp_f32_e32 v92, v92
	v_exp_f32_e32 v93, v93
	v_exp_f32_e32 v94, v94
	v_exp_f32_e32 v95, v95
	v_add_f32_e32 v68, v68, v69
	v_cvt_pk_fp8_f32 v101, v88, v89
	v_cvt_pk_fp8_f32 v101, v90, v91 op_sel:[0,0,1]
	v_fma_f32 v96, v96, v250, v251
	v_fma_f32 v97, v97, v250, v251
	v_fma_f32 v98, v98, v250, v251
	v_fma_f32 v99, v99, v250, v251
	v_add_f32_e32 v67, v67, v68
	v_add_f32_e32 v68, v92, v93
	v_add_f32_e32 v69, v94, v95
	s_waitcnt lgkmcnt(6)
	v_mfma_f32_32x32x64_f8f6f4 v[34:49], v[108:115], v[210:217], v[34:49]
	ds_read_b128 v[210:213], v191 offset:16384
	ds_read_b128 v[214:217], v192 offset:16384
	v_exp_f32_e32 v96, v96
	v_exp_f32_e32 v97, v97
	v_exp_f32_e32 v98, v98
	v_exp_f32_e32 v99, v99
	v_add_f32_e32 v68, v68, v69
	v_cvt_pk_fp8_f32 v102, v92, v93
	v_cvt_pk_fp8_f32 v102, v94, v95 op_sel:[0,0,1]
	v_add_f32_e32 v67, v67, v68
	v_add_f32_e32 v68, v96, v97
	v_add_f32_e32 v69, v98, v99
	s_add_u32 s60, s60, 0x4000
	s_addc_u32 s61, s61, 0
	v_add_f32_e32 v68, v68, v69
	v_cvt_pk_fp8_f32 v103, v96, v97
	v_cvt_pk_fp8_f32 v103, v98, v99 op_sel:[0,0,1]
	v_add_f32_e32 v67, v67, v68
	ds_write_b128 v194, v[100:103] offset:8192
	v_max_f32_e32 v72, v72, v67
	v_add_f32_e32 v66, v66, v67
	s_add_i32 s43, s43, 1
	s_waitcnt lgkmcnt(7)
	v_mfma_i32_32x32x32_i8 v[84:99], v[218:221], v[132:135], v[226:241]
	v_mfma_i32_32x32x32_i8 v[84:99], v[222:225], v[136:139], v[84:99]
	s_waitcnt vmcnt(2) lgkmcnt(0)
	s_barrier
.Lat_u3:
	ds_read_b128 v[104:107], v164 offset:8192
	v_mfma_i32_32x32x32_i8 v[84:99], v[242:245], v[140:143], v[84:99]
	ds_read_b128 v[116:119], v195 offset:6144
	ds_read_b128 v[120:123], v196 offset:6144
	s_add_i32 m0, s31, 49152
	ds_read_b128 v[124:127], v195 offset:4096
	global_load_lds_dwordx4 v252, s[60:61] nt
	s_add_i32 m0, s31, 57344
	v_mfma_i32_32x32x32_i8 v[84:99], v[246:249], v[144:147], v[84:99]
	global_load_lds_dwordx4 v254, s[60:61] nt
	ds_read_b128 v[128:131], v196 offset:4096
	v_mfma_i32_32x32x32_i8 v[84:99], v[202:205], v[148:151], v[84:99]
	ds_read_b128 v[202:205], v195
	v_mfma_i32_32x32x32_i8 v[84:99], v[206:209], v[152:155], v[84:99]
	ds_read_b128 v[206:209], v196
	v_mfma_i32_32x32x32_i8 v[84:99], v[210:213], v[156:159], v[84:99]
	ds_read_b128 v[210:213], v195 offset:2048
	v_mfma_i32_32x32x32_i8 v[84:99], v[214:217], v[160:163], v[84:99]
	ds_read_b128 v[214:217], v196 offset:2048
	v_readlane_b32 s50, v182, s43
	s_waitcnt lgkmcnt(6)
	v_mfma_f32_32x32x64_f8f6f4 v[2:17], v[100:107], v[116:123], v[2:17]
	ds_read_b128 v[218:221], v185 offset:32768
	ds_read_b128 v[222:225], v186 offset:32768
	ds_read_b128 v[242:245], v187 offset:32768
	ds_read_b128 v[246:249], v188 offset:32768
	v_mul_f32_e32 v250, s50, v71
	v_fmamk_f32 v251, v250, 0xcb400000, v200
	s_add_i32 m0, s31, 32768
	v_fma_f32 v84, v84, v250, v251
	global_load_lds_dwordx4 v255, s[60:61] nt
	s_add_i32 m0, s31, 40960
	v_fma_f32 v85, v85, v250, v251
	global_load_lds_dwordx4 v201, s[60:61] nt
	v_fma_f32 v86, v86, v250, v251
	v_fma_f32 v87, v87, v250, v251
	v_exp_f32_e32 v84, v84
	v_exp_f32_e32 v85, v85
	v_exp_f32_e32 v86, v86
	v_exp_f32_e32 v87, v87
	v_fma_f32 v88, v88, v250, v251
	v_fma_f32 v89, v89, v250, v251
	v_fma_f32 v90, v90, v250, v251
	v_fma_f32 v91, v91, v250, v251
	s_waitcnt lgkmcnt(8)
	v_mfma_f32_32x32x64_f8f6f4 v[18:33], v[100:107], v[124:131], v[18:33]
	v_add_f32_e32 v67, v84, v85
	v_add_f32_e32 v68, v86, v87
	v_exp_f32_e32 v88, v88
	v_exp_f32_e32 v89, v89
	v_exp_f32_e32 v90, v90
	v_exp_f32_e32 v91, v91
	v_add_f32_e32 v67, v67, v68
	v_cvt_pk_fp8_f32 v108, v84, v85
	v_cvt_pk_fp8_f32 v108, v86, v87 op_sel:[0,0,1]
	v_fma_f32 v92, v92, v250, v251
	v_fma_f32 v93, v93, v250, v251
	v_fma_f32 v94, v94, v250, v251
	v_fma_f32 v95, v95, v250, v251
	v_add_f32_e32 v68, v88, v89
	v_add_f32_e32 v69, v90, v91
	s_waitcnt lgkmcnt(6)
	v_mfma_f32_32x32x64_f8f6f4 v[50:65], v[100:107], v[202:209], v[50:65]
	ds_read_b128 v[202:205], v189 offset:32768
	ds_read_b128 v[206:209], v190 offset:32768
	v_exp_f32_e32 v92, v92
	v_exp_f32_e32 v93, v93
	v_exp_f32_e32 v94, v94
	v_exp_f32_e32 v95, v95
	v_add_f32_e32 v68, v68, v69
	v_cvt_pk_fp8_f32 v109, v88, v89
	v_cvt_pk_fp8_f32 v109, v90, v91 op_sel:[0,0,1]
	v_fma_f32 v96, v96, v250, v251
	v_fma_f32 v97, v97, v250, v251
	v_fma_f32 v98, v98, v250, v251
	v_fma_f32 v99, v99, v250, v251
	v_add_f32_e32 v67, v67, v68
	v_add_f32_e32 v68, v92, v93
	v_add_f32_e32 v69, v94, v95
	s_waitcnt lgkmcnt(6)
	v_mfma_f32_32x32x64_f8f6f4 v[34:49], v[100:107], v[210:217], v[34:49]
	ds_read_b128 v[210:213], v191 offset:32768
	ds_read_b128 v[214:217], v192 offset:32768
	v_exp_f32_e32 v96, v96
	v_exp_f32_e32 v97, v97
	v_exp_f32_e32 v98, v98
	v_exp_f32_e32 v99, v99
	v_add_f32_e32 v68, v68, v69
	v_cvt_pk_fp8_f32 v110, v92, v93
	v_cvt_pk_fp8_f32 v110, v94, v95 op_sel:[0,0,1]
	v_add_f32_e32 v67, v67, v68
	v_add_f32_e32 v68, v96, v97
	v_add_f32_e32 v69, v98, v99
	s_add_u32 s60, s60, 0x4000
	s_addc_u32 s61, s61, 0
	v_add_f32_e32 v68, v68, v69
	v_cvt_pk_fp8_f32 v111, v96, v97
	v_cvt_pk_fp8_f32 v111, v98, v99 op_sel:[0,0,1]
	v_add_f32_e32 v67, v67, v68
	ds_write_b128 v194, v[108:111]
	v_max_f32_e32 v72, v72, v67
	v_add_f32_e32 v66, v66, v67
	s_add_i32 s43, s43, 1
	s_waitcnt lgkmcnt(7)
	v_mfma_i32_32x32x32_i8 v[84:99], v[218:221], v[132:135], v[226:241]
	v_mfma_i32_32x32x32_i8 v[84:99], v[222:225], v[136:139], v[84:99]
	s_waitcnt vmcnt(2) lgkmcnt(0)
	s_barrier
.Lat_u4:
	ds_read_b128 v[112:115], v164
	v_mfma_i32_32x32x32_i8 v[84:99], v[242:245], v[140:143], v[84:99]
	ds_read_b128 v[116:119], v195 offset:22528
	ds_read_b128 v[120:123], v196 offset:22528
	s_add_i32 m0, s31, 65536
	ds_read_b128 v[124:127], v195 offset:20480
	global_load_lds_dwordx4 v252, s[60:61] nt
	s_add_i32 m0, s31, 73728
	v_mfma_i32_32x32x32_i8 v[84:99], v[246:249], v[144:147], v[84:99]
	global_load_lds_dwordx4 v254, s[60:61] nt
	ds_read_b128 v[128:131], v196 offset:20480
	v_mfma_i32_32x32x32_i8 v[84:99], v[202:205], v[148:151], v[84:99]
	ds_read_b128 v[202:205], v195 offset:16384
	v_mfma_i32_32x32x32_i8 v[84:99], v[206:209], v[152:155], v[84:99]
	ds_read_b128 v[206:209], v196 offset:16384
	v_mfma_i32_32x32x32_i8 v[84:99], v[210:213], v[156:159], v[84:99]
	ds_read_b128 v[210:213], v195 offset:18432
	v_mfma_i32_32x32x32_i8 v[84:99], v[214:217], v[160:163], v[84:99]
	ds_read_b128 v[214:217], v196 offset:18432
	v_readlane_b32 s50, v182, s43
	s_waitcnt lgkmcnt(6)
	v_mfma_f32_32x32x64_f8f6f4 v[2:17], v[108:115], v[116:123], v[2:17]
	ds_read_b128 v[218:221], v185
	ds_read_b128 v[222:225], v186
	ds_read_b128 v[242:245], v187
	ds_read_b128 v[246:249], v188
	v_mul_f32_e32 v250, s50, v71
	v_fmamk_f32 v251, v250, 0xcb400000, v200
	s_mov_b32 m0, s31
	v_fma_f32 v84, v84, v250, v251
	global_load_lds_dwordx4 v255, s[60:61] nt
	s_add_i32 m0, s31, 8192
	v_fma_f32 v85, v85, v250, v251
	global_load_lds_dwordx4 v201, s[60:61] nt
	v_fma_f32 v86, v86, v250, v251
	v_fma_f32 v87, v87, v250, v251
	v_exp_f32_e32 v84, v84
	v_exp_f32_e32 v85, v85
	v_exp_f32_e32 v86, v86
	v_exp_f32_e32 v87, v87
	v_fma_f32 v88, v88, v250, v251
	v_fma_f32 v89, v89, v250, v251
	v_fma_f32 v90, v90, v250, v251
	v_fma_f32 v91, v91, v250, v251
	s_waitcnt lgkmcnt(8)
	v_mfma_f32_32x32x64_f8f6f4 v[18:33], v[108:115], v[124:131], v[18:33]
	v_add_f32_e32 v67, v84, v85
	v_add_f32_e32 v68, v86, v87
	v_exp_f32_e32 v88, v88
	v_exp_f32_e32 v89, v89
	v_exp_f32_e32 v90, v90
	v_exp_f32_e32 v91, v91
	v_add_f32_e32 v67, v67, v68
	v_cvt_pk_fp8_f32 v100, v84, v85
	v_cvt_pk_fp8_f32 v100, v86, v87 op_sel:[0,0,1]
	v_fma_f32 v92, v92, v250, v251
	v_fma_f32 v93, v93, v250, v251
	v_fma_f32 v94, v94, v250, v251
	v_fma_f32 v95, v95, v250, v251
	v_add_f32_e32 v68, v88, v89
	v_add_f32_e32 v69, v90, v91
	s_waitcnt lgkmcnt(6)
	v_mfma_f32_32x32x64_f8f6f4 v[50:65], v[108:115], v[202:209], v[50:65]
	ds_read_b128 v[202:205], v189
	ds_read_b128 v[206:209], v190
	v_exp_f32_e32 v92, v92
	v_exp_f32_e32 v93, v93
	v_exp_f32_e32 v94, v94
	v_exp_f32_e32 v95, v95
	v_add_f32_e32 v68, v68, v69
	v_cvt_pk_fp8_f32 v101, v88, v89
	v_cvt_pk_fp8_f32 v101, v90, v91 op_sel:[0,0,1]
	v_fma_f32 v96, v96, v250, v251
	v_fma_f32 v97, v97, v250, v251
	v_fma_f32 v98, v98, v250, v251
	v_fma_f32 v99, v99, v250, v251
	v_add_f32_e32 v67, v67, v68
	v_add_f32_e32 v68, v92, v93
	v_add_f32_e32 v69, v94, v95
	s_waitcnt lgkmcnt(6)
	v_mfma_f32_32x32x64_f8f6f4 v[34:49], v[108:115], v[210:217], v[34:49]
	ds_read_b128 v[210:213], v191
	ds_read_b128 v[214:217], v192
	v_exp_f32_e32 v96, v96
	v_exp_f32_e32 v97, v97
	v_exp_f32_e32 v98, v98
	v_exp_f32_e32 v99, v99
	v_add_f32_e32 v68, v68, v69
	v_cvt_pk_fp8_f32 v102, v92, v93
	v_cvt_pk_fp8_f32 v102, v94, v95 op_sel:[0,0,1]
	v_add_f32_e32 v67, v67, v68
	v_add_f32_e32 v68, v96, v97
	v_add_f32_e32 v69, v98, v99
	s_add_u32 s60, s60, 0x4000
	s_addc_u32 s61, s61, 0
	v_add_f32_e32 v68, v68, v69
	v_cvt_pk_fp8_f32 v103, v96, v97
	v_cvt_pk_fp8_f32 v103, v98, v99 op_sel:[0,0,1]
	v_add_f32_e32 v67, v67, v68
	ds_write_b128 v194, v[100:103] offset:8192
	v_max_f32_e32 v72, v72, v67
	v_add_f32_e32 v66, v66, v67
	s_add_i32 s43, s43, 1
	s_waitcnt lgkmcnt(7)
	v_mfma_i32_32x32x32_i8 v[84:99], v[218:221], v[132:135], v[226:241]
	v_mfma_i32_32x32x32_i8 v[84:99], v[222:225], v[136:139], v[84:99]
	s_waitcnt vmcnt(2) lgkmcnt(0)
	s_barrier
.Lat_u5:
	ds_read_b128 v[104:107], v164 offset:8192
	v_mfma_i32_32x32x32_i8 v[84:99], v[242:245], v[140:143], v[84:99]
	ds_read_b128 v[116:119], v195 offset:38912
	ds_read_b128 v[120:123], v196 offset:38912
	s_cmp_gt_u32 s43, 29
	s_cbranch_scc1 .Lat_nok5
	s_add_i32 m0, s31, 81920
	ds_read_b128 v[124:127], v195 offset:36864
	global_load_lds_dwordx4 v252, s[60:61] nt
	s_add_i32 m0, s31, 90112
	v_mfma_i32_32x32x32_i8 v[84:99], v[246:249], v[144:147], v[84:99]
	global_load_lds_dwordx4 v254, s[60:61] nt
.Lat_k5:
	ds_read_b128 v[128:131], v196 offset:36864
	v_mfma_i32_32x32x32_i8 v[84:99], v[202:205], v[148:151], v[84:99]
	ds_read_b128 v[202:205], v195 offset:32768
	v_mfma_i32_32x32x32_i8 v[84:99], v[206:209], v[152:155], v[84:99]
	ds_read_b128 v[206:209], v196 offset:32768
	v_mfma_i32_32x32x32_i8 v[84:99], v[210:213], v[156:159], v[84:99]
	ds_read_b128 v[210:213], v195 offset:34816
	v_mfma_i32_32x32x32_i8 v[84:99], v[214:217], v[160:163], v[84:99]
	ds_read_b128 v[214:217], v196 offset:34816
	v_readlane_b32 s50, v182, s43
	s_waitcnt lgkmcnt(6)
	v_mfma_f32_32x32x64_f8f6f4 v[2:17], v[100:107], v[116:123], v[2:17]
	ds_read_b128 v[218:221], v185 offset:16384
	ds_read_b128 v[222:225], v186 offset:16384
	ds_read_b128 v[242:245], v187 offset:16384
	ds_read_b128 v[246:249], v188 offset:16384
	v_mul_f32_e32 v250, s50, v71
	v_fmamk_f32 v251, v250, 0xcb400000, v200
	s_add_i32 m0, s31, 16384
	v_fma_f32 v84, v84, v250, v251
	global_load_lds_dwordx4 v255, s[60:61] nt
	s_add_i32 m0, s31, 24576
	v_fma_f32 v85, v85, v250, v251
	global_load_lds_dwordx4 v201, s[60:61] nt
	v_fma_f32 v86, v86, v250, v251
	v_fma_f32 v87, v87, v250, v251
	v_exp_f32_e32 v84, v84
	v_exp_f32_e32 v85, v85
	v_exp_f32_e32 v86, v86
	v_exp_f32_e32 v87, v87
	v_fma_f32 v88, v88, v250, v251
	v_fma_f32 v89, v89, v250, v251
	v_fma_f32 v90, v90, v250, v251
	v_fma_f32 v91, v91, v250, v251
	s_waitcnt lgkmcnt(8)
	v_mfma_f32_32x32x64_f8f6f4 v[18:33], v[100:107], v[124:131], v[18:33]
	v_add_f32_e32 v67, v84, v85
	v_add_f32_e32 v68, v86, v87
	v_exp_f32_e32 v88, v88
	v_exp_f32_e32 v89, v89
	v_exp_f32_e32 v90, v90
	v_exp_f32_e32 v91, v91
	v_add_f32_e32 v67, v67, v68
	v_cvt_pk_fp8_f32 v108, v84, v85
	v_cvt_pk_fp8_f32 v108, v86, v87 op_sel:[0,0,1]
	v_fma_f32 v92, v92, v250, v251
	v_fma_f32 v93, v93, v250, v251
	v_fma_f32 v94, v94, v250, v251
	v_fma_f32 v95, v95, v250, v251
	v_add_f32_e32 v68, v88, v89
	v_add_f32_e32 v69, v90, v91
	s_waitcnt lgkmcnt(6)
	v_mfma_f32_32x32x64_f8f6f4 v[50:65], v[100:107], v[202:209], v[50:65]
	ds_read_b128 v[202:205], v189 offset:16384
	ds_read_b128 v[206:209], v190 offset:16384
	v_exp_f32_e32 v92, v92
	v_exp_f32_e32 v93, v93
	v_exp_f32_e32 v94, v94
	v_exp_f32_e32 v95, v95
	v_add_f32_e32 v68, v68, v69
	v_cvt_pk_fp8_f32 v109, v88, v89
	v_cvt_pk_fp8_f32 v109, v90, v91 op_sel:[0,0,1]
	v_fma_f32 v96, v96, v250, v251
	v_fma_f32 v97, v97, v250, v251
	v_fma_f32 v98, v98, v250, v251
	v_fma_f32 v99, v99, v250, v251
	v_add_f32_e32 v67, v67, v68
	v_add_f32_e32 v68, v92, v93
	v_add_f32_e32 v69, v94, v95
	s_waitcnt lgkmcnt(6)
	v_mfma_f32_32x32x64_f8f6f4 v[34:49], v[100:107], v[210:217], v[34:49]
	ds_read_b128 v[210:213], v191 offset:16384
	ds_read_b128 v[214:217], v192 offset:16384
	v_exp_f32_e32 v96, v96
	v_exp_f32_e32 v97, v97
	v_exp_f32_e32 v98, v98
	v_exp_f32_e32 v99, v99
	v_add_f32_e32 v68, v68, v69
	v_cvt_pk_fp8_f32 v110, v92, v93
	v_cvt_pk_fp8_f32 v110, v94, v95 op_sel:[0,0,1]
	v_add_f32_e32 v67, v67, v68
	v_add_f32_e32 v68, v96, v97
	v_add_f32_e32 v69, v98, v99
	s_add_u32 s60, s60, 0x4000
	s_addc_u32 s61, s61, 0
	v_add_f32_e32 v68, v68, v69
	v_cvt_pk_fp8_f32 v111, v96, v97
	v_cvt_pk_fp8_f32 v111, v98, v99 op_sel:[0,0,1]
	v_add_f32_e32 v67, v67, v68
	ds_write_b128 v194, v[108:111]
	v_max_f32_e32 v72, v72, v67
	v_add_f32_e32 v66, v66, v67
	s_add_i32 s43, s43, 1
	s_waitcnt lgkmcnt(7)
	v_mfma_i32_32x32x32_i8 v[84:99], v[218:221], v[132:135], v[226:241]
	v_mfma_i32_32x32x32_i8 v[84:99], v[222:225], v[136:139], v[84:99]
	s_cmp_gt_u32 s43, 30
	s_cbranch_scc1 .Lat_drain
	s_waitcnt vmcnt(2) lgkmcnt(0)
	s_barrier
	s_branch .Lat_u0
